# bf16 GEMM K-loops of in-proj, dense gate/up, dense down: the two ds_read address adds that head the SP1/SP3 load blocks hoisted in front of the opening barrier (loop bottom + pre-header copy)
# speedup vs baseline: 1.0076x; 1.0076x over previous
; template <class P, bool ALIGN_EPI>
; __device__ __forceinline__ void gemm_phase(ldsp lds, ldsp tab, const P& S) {
;     ...
;         if constexpr (!P::FP8) {
; #pragma unroll
;             for (int a = 0; a < 2; ++a)
; #pragma unroll
;                 for (int b = 0; b < 2; ++b)
; #pragma unroll
;                     for (int m = 0; m < 4; ++m)
; #pragma unroll
;                         for (int n = 0; n < 2; ++n) acc[a][b][m][n] = (f32x4){0.f, 0.f, 0.f, 0.f}; }
.LBB0_846:
	s_ashr_i32 s17, s16, 31
	s_lshl_b64 s[18:19], s[16:17], 19
	s_add_u32 s18, s50, s18
	s_addc_u32 s19, s51, s19
	s_ashr_i32 s15, s14, 31
	s_lshl_b64 s[20:21], s[14:15], 19
	s_add_u32 s20, s52, s20
	v_mov_b32_e32 v4, 0
	s_addc_u32 s21, s53, s21
	s_mov_b32 s3, -2
	s_mov_b64 s[38:39], 0x40080
	v_mov_b32_e32 v5, v4
	v_mov_b32_e32 v6, v4
	v_mov_b32_e32 v7, v4
	v_mov_b32_e32 v8, v4
	v_mov_b32_e32 v9, v4
	v_mov_b32_e32 v10, v4
	v_mov_b32_e32 v11, v4
	v_mov_b32_e32 v20, v4
	v_mov_b32_e32 v21, v4
	v_mov_b32_e32 v22, v4
	v_mov_b32_e32 v23, v4
	v_mov_b32_e32 v24, v4
	v_mov_b32_e32 v25, v4
	v_mov_b32_e32 v26, v4
	v_mov_b32_e32 v27, v4
	v_mov_b32_e32 v36, v4
	v_mov_b32_e32 v37, v4
	v_mov_b32_e32 v38, v4
	v_mov_b32_e32 v39, v4
	v_mov_b32_e32 v40, v4
	v_mov_b32_e32 v41, v4
	v_mov_b32_e32 v42, v4
	v_mov_b32_e32 v43, v4
	v_mov_b32_e32 v52, v4
	v_mov_b32_e32 v53, v4
	v_mov_b32_e32 v54, v4
	v_mov_b32_e32 v55, v4
	v_mov_b32_e32 v56, v4
	v_mov_b32_e32 v57, v4
	v_mov_b32_e32 v58, v4
	v_mov_b32_e32 v59, v4
	v_mov_b32_e32 v12, v4
	v_mov_b32_e32 v13, v4
	v_mov_b32_e32 v14, v4
	v_mov_b32_e32 v15, v4
	v_mov_b32_e32 v16, v4
	v_mov_b32_e32 v17, v4
	v_mov_b32_e32 v18, v4
	v_mov_b32_e32 v19, v4
	v_mov_b32_e32 v28, v4
	v_mov_b32_e32 v29, v4
	v_mov_b32_e32 v30, v4
	v_mov_b32_e32 v31, v4
	v_mov_b32_e32 v32, v4
	v_mov_b32_e32 v33, v4
	v_mov_b32_e32 v34, v4
	v_mov_b32_e32 v35, v4
	v_mov_b32_e32 v44, v4
	v_mov_b32_e32 v45, v4
	v_mov_b32_e32 v46, v4
	v_mov_b32_e32 v47, v4
	v_mov_b32_e32 v48, v4
	v_mov_b32_e32 v49, v4
	v_mov_b32_e32 v50, v4
	v_mov_b32_e32 v51, v4
	v_mov_b32_e32 v60, v4
	v_mov_b32_e32 v61, v4
	v_mov_b32_e32 v62, v4
	v_mov_b32_e32 v63, v4
	v_mov_b32_e32 v64, v4
	v_mov_b32_e32 v65, v4
	v_mov_b32_e32 v66, v4
	v_mov_b32_e32 v67, v4
	v_mov_b32_e32 v80, v4
	v_mov_b32_e32 v81, v4
	v_mov_b32_e32 v82, v4
	v_mov_b32_e32 v83, v4
	v_mov_b32_e32 v88, v4
	v_mov_b32_e32 v89, v4
	v_mov_b32_e32 v90, v4
	v_mov_b32_e32 v91, v4
	v_mov_b32_e32 v108, v4
	v_mov_b32_e32 v109, v4
	v_mov_b32_e32 v110, v4
	v_mov_b32_e32 v111, v4
	v_mov_b32_e32 v112, v4
	v_mov_b32_e32 v113, v4
	v_mov_b32_e32 v114, v4
	v_mov_b32_e32 v115, v4
	v_mov_b32_e32 v132, v4
	v_mov_b32_e32 v133, v4
	v_mov_b32_e32 v134, v4
	v_mov_b32_e32 v135, v4
	v_mov_b32_e32 v136, v4
	v_mov_b32_e32 v137, v4
	v_mov_b32_e32 v138, v4
	v_mov_b32_e32 v139, v4
	v_mov_b32_e32 v156, v4
	v_mov_b32_e32 v157, v4
	v_mov_b32_e32 v158, v4
	v_mov_b32_e32 v159, v4
	v_mov_b32_e32 v160, v4
	v_mov_b32_e32 v161, v4
	v_mov_b32_e32 v162, v4
	v_mov_b32_e32 v163, v4
	v_mov_b32_e32 v96, v4
	v_mov_b32_e32 v97, v4
	v_mov_b32_e32 v98, v4
	v_mov_b32_e32 v99, v4
	v_mov_b32_e32 v104, v4
	v_mov_b32_e32 v105, v4
	v_mov_b32_e32 v106, v4
	v_mov_b32_e32 v107, v4
	v_mov_b32_e32 v120, v4
	v_mov_b32_e32 v121, v4
	v_mov_b32_e32 v122, v4
	v_mov_b32_e32 v123, v4
	v_mov_b32_e32 v124, v4
	v_mov_b32_e32 v125, v4
	v_mov_b32_e32 v126, v4
	v_mov_b32_e32 v127, v4
	v_mov_b32_e32 v144, v4
	v_mov_b32_e32 v145, v4
	v_mov_b32_e32 v146, v4
	v_mov_b32_e32 v147, v4
	v_mov_b32_e32 v148, v4
	v_mov_b32_e32 v149, v4
	v_mov_b32_e32 v150, v4
	v_mov_b32_e32 v151, v4
	v_mov_b32_e32 v168, v4
	v_mov_b32_e32 v169, v4
	v_mov_b32_e32 v170, v4
	v_mov_b32_e32 v171, v4
	v_mov_b32_e32 v176, v4
	v_mov_b32_e32 v177, v4
	v_mov_b32_e32 v178, v4
	v_mov_b32_e32 v179, v4
	v_add_u32_e32 v84, 0x10000, v231
	v_add_u32_e32 v128, 0x14000, v231
.LBB0_847:
	ds_read_b128 v[68:71], v84
	ds_read_b128 v[72:75], v84 offset:1024
	ds_read_b128 v[76:79], v84 offset:2048
	ds_read_b128 v[84:87], v84 offset:3072
	ds_read_b128 v[92:95], v128
	ds_read_b128 v[100:103], v128 offset:1024
	ds_read_b128 v[116:119], v128 offset:2048
	ds_read_b128 v[128:131], v128 offset:3072
	ds_read_b128 v[140:143], v232
	ds_read_b128 v[152:155], v232 offset:1024
	ds_read_b128 v[164:167], v232 offset:2048
	ds_read_b128 v[172:175], v232 offset:3072
	ds_read_b128 v[180:183], v232 offset:4096
	ds_read_b128 v[184:187], v232 offset:5120
	ds_read_b128 v[188:191], v232 offset:6144
	ds_read_b128 v[192:195], v232 offset:7168
	s_add_u32 s15, s38, 0xfffc0080
	s_addc_u32 s17, s39, -1
	s_cmp_eq_u32 s3, 12
	s_cselect_b64 s[26:27], -1, 0
	s_and_b64 s[34:35], s[26:27], exec
	s_cselect_b32 s17, 0, s17
	s_cselect_b32 s15, 0, s15
	s_and_b64 s[26:27], s[26:27], s[36:37]
	s_and_b64 s[34:35], s[26:27], exec
	s_cselect_b32 s28, s20, s30
	s_cselect_b32 s23, s21, s31
	s_add_u32 s42, s28, s15
	s_addc_u32 s43, s23, s17
	s_add_i32 s23, 0, 0x10000
	s_and_b64 s[26:27], s[26:27], exec
	s_cselect_b32 s28, s19, s1
	s_cselect_b32 s33, s18, s0
	s_add_i32 s34, 0, 0x14000
	s_add_i32 m0, s55, 0xc000
	s_add_u32 s26, s0, s38
	s_addc_u32 s27, s1, s39
	global_load_lds_dwordx4 v2, s[26:27]
	s_add_i32 m0, s55, 0xe000
	v_mov_b32_e32 v219, v3
	global_load_lds_dwordx4 v218, s[26:27]
	s_waitcnt vmcnt(8)
	s_waitcnt lgkmcnt(0)
	s_barrier
	s_setprio 1
	s_waitcnt lgkmcnt(0)
	v_mfma_f32_16x16x32_bf16 v[176:179], v[68:71], v[140:143], v[176:179]
	v_mfma_f32_16x16x32_bf16 v[168:171], v[76:79], v[140:143], v[168:171]
	v_mfma_f32_16x16x32_bf16 v[148:151], v[68:71], v[164:167], v[148:151]
	v_mfma_f32_16x16x32_bf16 v[144:147], v[76:79], v[164:167], v[144:147]
	v_mfma_f32_16x16x32_bf16 v[124:127], v[68:71], v[180:183], v[124:127]
	v_mfma_f32_16x16x32_bf16 v[120:123], v[76:79], v[180:183], v[120:123]
	v_mfma_f32_16x16x32_bf16 v[104:107], v[68:71], v[188:191], v[104:107]
	v_mfma_f32_16x16x32_bf16 v[96:99], v[76:79], v[188:191], v[96:99]
	v_mfma_f32_16x16x32_bf16 v[176:179], v[72:75], v[152:155], v[176:179]
	v_mfma_f32_16x16x32_bf16 v[168:171], v[84:87], v[152:155], v[168:171]
	v_mfma_f32_16x16x32_bf16 v[148:151], v[72:75], v[172:175], v[148:151]
	v_mfma_f32_16x16x32_bf16 v[144:147], v[84:87], v[172:175], v[144:147]
	v_mfma_f32_16x16x32_bf16 v[124:127], v[72:75], v[184:187], v[124:127]
	v_mfma_f32_16x16x32_bf16 v[120:123], v[84:87], v[184:187], v[120:123]
	v_mfma_f32_16x16x32_bf16 v[104:107], v[72:75], v[192:195], v[104:107]
	v_mfma_f32_16x16x32_bf16 v[96:99], v[84:87], v[192:195], v[96:99]
	s_setprio 0
	s_setprio 1
	v_mfma_f32_16x16x32_bf16 v[160:163], v[92:95], v[140:143], v[160:163]
	v_mfma_f32_16x16x32_bf16 v[136:139], v[92:95], v[164:167], v[136:139]
	v_mfma_f32_16x16x32_bf16 v[132:135], v[116:119], v[164:167], v[132:135]
	v_mfma_f32_16x16x32_bf16 v[112:115], v[92:95], v[180:183], v[112:115]
	v_mfma_f32_16x16x32_bf16 v[108:111], v[116:119], v[180:183], v[108:111]
	v_mfma_f32_16x16x32_bf16 v[88:91], v[92:95], v[188:191], v[88:91]
	v_mfma_f32_16x16x32_bf16 v[80:83], v[116:119], v[188:191], v[80:83]
	v_mfma_f32_16x16x32_bf16 v[160:163], v[100:103], v[152:155], v[160:163]
	v_mfma_f32_16x16x32_bf16 v[140:143], v[116:119], v[140:143], v[156:159]
	v_mfma_f32_16x16x32_bf16 v[136:139], v[100:103], v[172:175], v[136:139]
	v_mfma_f32_16x16x32_bf16 v[132:135], v[128:131], v[172:175], v[132:135]
	v_mfma_f32_16x16x32_bf16 v[112:115], v[100:103], v[184:187], v[112:115]
	v_mfma_f32_16x16x32_bf16 v[108:111], v[128:131], v[184:187], v[108:111]
	v_mfma_f32_16x16x32_bf16 v[88:91], v[100:103], v[192:195], v[88:91]
	v_mfma_f32_16x16x32_bf16 v[80:83], v[128:131], v[192:195], v[80:83]
	v_mfma_f32_16x16x32_bf16 v[140:143], v[128:131], v[152:155], v[140:143]
	s_setprio 0
	s_barrier
	ds_read_b128 v[152:155], v232 offset:16384
	ds_read_b128 v[156:159], v232 offset:17408
	ds_read_b128 v[164:167], v232 offset:18432
	ds_read_b128 v[172:175], v232 offset:19456
	ds_read_b128 v[180:183], v232 offset:20480
	ds_read_b128 v[184:187], v232 offset:21504
	ds_read_b128 v[188:191], v232 offset:22528
	ds_read_b128 v[192:195], v232 offset:23552
	s_add_i32 s23, s23, s54
	s_mov_b32 m0, s23
	global_load_lds_dwordx4 v216, s[42:43]
	s_add_i32 m0, s23, 0x2000
	s_add_u32 s26, s42, 0x40000
	s_addc_u32 s27, s43, 0
	s_add_i32 s23, s34, s54
	global_load_lds_dwordx4 v220, s[42:43]
	s_mov_b32 m0, s23
	v_mov_b32_e32 v217, v3
	global_load_lds_dwordx4 v216, s[26:27]
	s_add_i32 m0, s23, 0x2000
	v_mov_b32_e32 v221, v3
	global_load_lds_dwordx4 v220, s[26:27]
	s_add_u32 s26, s33, s15
	s_addc_u32 s27, s28, s17
	s_mov_b32 m0, s55
	v_lshl_add_u64 v[196:197], s[42:43], 0, v[216:217]
	global_load_lds_dwordx4 v2, s[26:27]
	s_mov_b32 m0, s56
	v_lshl_add_u64 v[198:199], s[42:43], 0, v[220:221]
	global_load_lds_dwordx4 v218, s[26:27]
	s_waitcnt vmcnt(8)
	s_waitcnt lgkmcnt(0)
	v_lshl_add_u64 v[200:201], s[26:27], 0, v[2:3]
	v_lshl_add_u64 v[202:203], s[26:27], 0, v[218:219]
	s_barrier
	s_setprio 1
	s_waitcnt lgkmcnt(0)
	v_mfma_f32_16x16x32_bf16 v[64:67], v[68:71], v[152:155], v[64:67]
	v_mfma_f32_16x16x32_bf16 v[60:63], v[76:79], v[152:155], v[60:63]
	v_mfma_f32_16x16x32_bf16 v[48:51], v[68:71], v[164:167], v[48:51]
	v_mfma_f32_16x16x32_bf16 v[44:47], v[76:79], v[164:167], v[44:47]
	v_mfma_f32_16x16x32_bf16 v[32:35], v[68:71], v[180:183], v[32:35]
	v_mfma_f32_16x16x32_bf16 v[28:31], v[76:79], v[180:183], v[28:31]
	v_mfma_f32_16x16x32_bf16 v[16:19], v[68:71], v[188:191], v[16:19]
	v_mfma_f32_16x16x32_bf16 v[12:15], v[76:79], v[188:191], v[12:15]
	v_mfma_f32_16x16x32_bf16 v[64:67], v[72:75], v[156:159], v[64:67]
	v_mfma_f32_16x16x32_bf16 v[60:63], v[84:87], v[156:159], v[60:63]
	v_mfma_f32_16x16x32_bf16 v[48:51], v[72:75], v[172:175], v[48:51]
	v_mfma_f32_16x16x32_bf16 v[44:47], v[84:87], v[172:175], v[44:47]
	v_mfma_f32_16x16x32_bf16 v[32:35], v[72:75], v[184:187], v[32:35]
	v_mfma_f32_16x16x32_bf16 v[28:31], v[84:87], v[184:187], v[28:31]
	v_mfma_f32_16x16x32_bf16 v[16:19], v[72:75], v[192:195], v[16:19]
	v_mfma_f32_16x16x32_bf16 v[12:15], v[84:87], v[192:195], v[12:15]
	s_setprio 0
	s_setprio 1
	v_mfma_f32_16x16x32_bf16 v[56:59], v[92:95], v[152:155], v[56:59]
	v_mfma_f32_16x16x32_bf16 v[52:55], v[116:119], v[152:155], v[52:55]
	v_mfma_f32_16x16x32_bf16 v[40:43], v[92:95], v[164:167], v[40:43]
	v_mfma_f32_16x16x32_bf16 v[36:39], v[116:119], v[164:167], v[36:39]
	v_mfma_f32_16x16x32_bf16 v[24:27], v[92:95], v[180:183], v[24:27]
	v_mfma_f32_16x16x32_bf16 v[20:23], v[116:119], v[180:183], v[20:23]
	v_mfma_f32_16x16x32_bf16 v[8:11], v[92:95], v[188:191], v[8:11]
	v_mfma_f32_16x16x32_bf16 v[4:7], v[116:119], v[188:191], v[4:7]
	v_mfma_f32_16x16x32_bf16 v[56:59], v[100:103], v[156:159], v[56:59]
	v_mfma_f32_16x16x32_bf16 v[52:55], v[128:131], v[156:159], v[52:55]
	v_mfma_f32_16x16x32_bf16 v[40:43], v[100:103], v[172:175], v[40:43]
	v_mfma_f32_16x16x32_bf16 v[36:39], v[128:131], v[172:175], v[36:39]
	v_mfma_f32_16x16x32_bf16 v[24:27], v[100:103], v[184:187], v[24:27]
	v_mfma_f32_16x16x32_bf16 v[20:23], v[128:131], v[184:187], v[20:23]
	v_mfma_f32_16x16x32_bf16 v[8:11], v[100:103], v[192:195], v[8:11]
	v_mfma_f32_16x16x32_bf16 v[4:7], v[128:131], v[192:195], v[4:7]
	v_add_u32_e32 v84, 0x18000, v231
	v_add_u32_e32 v128, 0x1c000, v231
	s_setprio 0
	s_barrier
; template <class P, bool ALIGN_EPI>
; __device__ __forceinline__ void gemm_phase(ldsp lds, ldsp tab, const P& S) {
;     ...
;             for (int t = 2; t < nt; t += 2) PG8_TRIP(t, PG8_MMA);
;         } else {
;             for (int t = 0; t < nt; t += 2) PG8_TRIP(t, PG8_MMA);
	ds_read_b128 v[68:71], v84
	ds_read_b128 v[72:75], v84 offset:1024
	ds_read_b128 v[76:79], v84 offset:2048
	ds_read_b128 v[84:87], v84 offset:3072
	ds_read_b128 v[92:95], v128
	ds_read_b128 v[100:103], v128 offset:1024
	ds_read_b128 v[116:119], v128 offset:2048
	ds_read_b128 v[128:131], v128 offset:3072
	ds_read_b128 v[152:155], v232 offset:32768
	ds_read_b128 v[156:159], v232 offset:33792
	ds_read_b128 v[164:167], v232 offset:34816
	ds_read_b128 v[172:175], v232 offset:35840
	ds_read_b128 v[180:183], v232 offset:36864
	ds_read_b128 v[184:187], v232 offset:37888
	ds_read_b128 v[188:191], v232 offset:38912
	ds_read_b128 v[192:195], v232 offset:39936
	s_add_i32 s15, 0, 0x18000
	s_add_i32 s17, 0, 0x1c000
	s_add_u32 s26, s26, 0x40000
	s_addc_u32 s27, s27, 0
	s_mov_b32 m0, s57
	global_load_lds_dwordx4 v2, s[26:27]
	s_mov_b32 m0, s58
	s_nop 0
	global_load_lds_dwordx4 v218, s[26:27]
	s_waitcnt vmcnt(8)
	s_waitcnt lgkmcnt(0)
	s_barrier
	s_setprio 1
	s_waitcnt lgkmcnt(0)
	v_mfma_f32_16x16x32_bf16 v[176:179], v[68:71], v[152:155], v[176:179]
	v_mfma_f32_16x16x32_bf16 v[168:171], v[76:79], v[152:155], v[168:171]
	v_mfma_f32_16x16x32_bf16 v[148:151], v[68:71], v[164:167], v[148:151]
	v_mfma_f32_16x16x32_bf16 v[144:147], v[76:79], v[164:167], v[144:147]
	v_mfma_f32_16x16x32_bf16 v[124:127], v[68:71], v[180:183], v[124:127]
	v_mfma_f32_16x16x32_bf16 v[120:123], v[76:79], v[180:183], v[120:123]
	v_mfma_f32_16x16x32_bf16 v[104:107], v[68:71], v[188:191], v[104:107]
	v_mfma_f32_16x16x32_bf16 v[96:99], v[76:79], v[188:191], v[96:99]
	v_mfma_f32_16x16x32_bf16 v[176:179], v[72:75], v[156:159], v[176:179]
	v_mfma_f32_16x16x32_bf16 v[168:171], v[84:87], v[156:159], v[168:171]
	v_mfma_f32_16x16x32_bf16 v[148:151], v[72:75], v[172:175], v[148:151]
	v_mfma_f32_16x16x32_bf16 v[144:147], v[84:87], v[172:175], v[144:147]
	v_mfma_f32_16x16x32_bf16 v[124:127], v[72:75], v[184:187], v[124:127]
	v_mfma_f32_16x16x32_bf16 v[120:123], v[84:87], v[184:187], v[120:123]
	v_mfma_f32_16x16x32_bf16 v[104:107], v[72:75], v[192:195], v[104:107]
	v_mfma_f32_16x16x32_bf16 v[96:99], v[84:87], v[192:195], v[96:99]
	s_setprio 0
	s_setprio 1
	v_mfma_f32_16x16x32_bf16 v[160:163], v[92:95], v[152:155], v[160:163]
	v_mfma_f32_16x16x32_bf16 v[140:143], v[116:119], v[152:155], v[140:143]
	v_mfma_f32_16x16x32_bf16 v[136:139], v[92:95], v[164:167], v[136:139]
	v_mfma_f32_16x16x32_bf16 v[132:135], v[116:119], v[164:167], v[132:135]
	v_mfma_f32_16x16x32_bf16 v[112:115], v[92:95], v[180:183], v[112:115]
	v_mfma_f32_16x16x32_bf16 v[108:111], v[116:119], v[180:183], v[108:111]
	v_mfma_f32_16x16x32_bf16 v[88:91], v[92:95], v[188:191], v[88:91]
	v_mfma_f32_16x16x32_bf16 v[80:83], v[116:119], v[188:191], v[80:83]
	v_mfma_f32_16x16x32_bf16 v[160:163], v[100:103], v[156:159], v[160:163]
	v_mfma_f32_16x16x32_bf16 v[156:159], v[128:131], v[156:159], v[140:143]
	v_mfma_f32_16x16x32_bf16 v[136:139], v[100:103], v[172:175], v[136:139]
	v_mfma_f32_16x16x32_bf16 v[132:135], v[128:131], v[172:175], v[132:135]
	v_mfma_f32_16x16x32_bf16 v[112:115], v[100:103], v[184:187], v[112:115]
	v_mfma_f32_16x16x32_bf16 v[108:111], v[128:131], v[184:187], v[108:111]
	v_mfma_f32_16x16x32_bf16 v[88:91], v[100:103], v[192:195], v[88:91]
	v_mfma_f32_16x16x32_bf16 v[80:83], v[128:131], v[192:195], v[80:83]
	s_setprio 0
	s_barrier
	ds_read_b128 v[140:143], v232 offset:49152
	ds_read_b128 v[152:155], v232 offset:50176
	ds_read_b128 v[164:167], v232 offset:51200
	ds_read_b128 v[172:175], v232 offset:52224
	ds_read_b128 v[180:183], v232 offset:53248
	ds_read_b128 v[184:187], v232 offset:54272
	ds_read_b128 v[188:191], v232 offset:55296
	ds_read_b128 v[192:195], v232 offset:56320
	s_add_i32 s15, s15, s54
	v_lshl_add_u64 v[196:197], v[196:197], 0, s[24:25]
	s_mov_b32 m0, s15
	global_load_lds_dwordx4 v[196:197], off
	s_add_i32 m0, s15, 0x2000
	s_add_u32 s26, s42, 0x40080
	v_lshl_add_u64 v[196:197], v[198:199], 0, s[24:25]
	s_addc_u32 s27, s43, 0
	s_add_i32 s15, s17, s54
	global_load_lds_dwordx4 v[196:197], off
	s_mov_b32 m0, s15
	v_lshl_add_u64 v[196:197], v[200:201], 0, s[24:25]
	global_load_lds_dwordx4 v216, s[26:27]
	s_add_i32 m0, s15, 0x2000
	s_nop 0
	global_load_lds_dwordx4 v220, s[26:27]
	s_mov_b32 m0, s60
	s_nop 0
	global_load_lds_dwordx4 v[196:197], off
	v_lshl_add_u64 v[196:197], v[202:203], 0, s[24:25]
	s_mov_b32 m0, s61
	s_nop 0
	global_load_lds_dwordx4 v[196:197], off
	s_waitcnt vmcnt(8)
	s_waitcnt lgkmcnt(0)
	s_barrier
	s_setprio 1
	s_waitcnt lgkmcnt(0)
	v_mfma_f32_16x16x32_bf16 v[64:67], v[68:71], v[140:143], v[64:67]
	v_mfma_f32_16x16x32_bf16 v[60:63], v[76:79], v[140:143], v[60:63]
	v_mfma_f32_16x16x32_bf16 v[48:51], v[68:71], v[164:167], v[48:51]
	v_mfma_f32_16x16x32_bf16 v[44:47], v[76:79], v[164:167], v[44:47]
	v_mfma_f32_16x16x32_bf16 v[32:35], v[68:71], v[180:183], v[32:35]
	v_mfma_f32_16x16x32_bf16 v[28:31], v[76:79], v[180:183], v[28:31]
	v_mfma_f32_16x16x32_bf16 v[16:19], v[68:71], v[188:191], v[16:19]
	v_mfma_f32_16x16x32_bf16 v[12:15], v[76:79], v[188:191], v[12:15]
	v_mfma_f32_16x16x32_bf16 v[64:67], v[72:75], v[152:155], v[64:67]
	v_mfma_f32_16x16x32_bf16 v[60:63], v[84:87], v[152:155], v[60:63]
	v_mfma_f32_16x16x32_bf16 v[48:51], v[72:75], v[172:175], v[48:51]
	v_mfma_f32_16x16x32_bf16 v[44:47], v[84:87], v[172:175], v[44:47]
	v_mfma_f32_16x16x32_bf16 v[32:35], v[72:75], v[184:187], v[32:35]
	v_mfma_f32_16x16x32_bf16 v[28:31], v[84:87], v[184:187], v[28:31]
	v_mfma_f32_16x16x32_bf16 v[16:19], v[72:75], v[192:195], v[16:19]
	v_mfma_f32_16x16x32_bf16 v[12:15], v[84:87], v[192:195], v[12:15]
	s_setprio 0
	s_setprio 1
	v_mfma_f32_16x16x32_bf16 v[56:59], v[92:95], v[140:143], v[56:59]
	v_mfma_f32_16x16x32_bf16 v[52:55], v[116:119], v[140:143], v[52:55]
	v_mfma_f32_16x16x32_bf16 v[40:43], v[92:95], v[164:167], v[40:43]
	v_mfma_f32_16x16x32_bf16 v[36:39], v[116:119], v[164:167], v[36:39]
	v_mfma_f32_16x16x32_bf16 v[24:27], v[92:95], v[180:183], v[24:27]
	v_mfma_f32_16x16x32_bf16 v[20:23], v[116:119], v[180:183], v[20:23]
	v_mfma_f32_16x16x32_bf16 v[8:11], v[92:95], v[188:191], v[8:11]
	v_mfma_f32_16x16x32_bf16 v[4:7], v[116:119], v[188:191], v[4:7]
	v_mfma_f32_16x16x32_bf16 v[56:59], v[100:103], v[152:155], v[56:59]
	v_mfma_f32_16x16x32_bf16 v[52:55], v[128:131], v[152:155], v[52:55]
	v_mfma_f32_16x16x32_bf16 v[40:43], v[100:103], v[172:175], v[40:43]
	v_mfma_f32_16x16x32_bf16 v[36:39], v[128:131], v[172:175], v[36:39]
	v_mfma_f32_16x16x32_bf16 v[24:27], v[100:103], v[184:187], v[24:27]
	v_mfma_f32_16x16x32_bf16 v[20:23], v[128:131], v[184:187], v[20:23]
	v_mfma_f32_16x16x32_bf16 v[8:11], v[100:103], v[192:195], v[8:11]
	v_mfma_f32_16x16x32_bf16 v[4:7], v[128:131], v[192:195], v[4:7]
	v_add_u32_e32 v84, 0x10000, v231
	v_add_u32_e32 v128, 0x14000, v231
	s_setprio 0
	s_barrier
	s_add_i32 s3, s3, 2
	s_add_u32 s38, s38, 0x100
	s_addc_u32 s39, s39, 0
	s_cmp_gt_u32 s3, 13
	s_cbranch_scc0 .LBB0_847
	s_and_b64 vcc, exec, s[10:11]
	s_cbranch_vccz .LBB0_850
	s_barrier

; template <class P, bool ALIGN_EPI>
; __device__ __forceinline__ void gemm_phase(ldsp lds, ldsp tab, const P& S) {
;     ...
;         if constexpr (!P::FP8) {
; #pragma unroll
;             for (int a = 0; a < 2; ++a)
; #pragma unroll
;                 for (int b = 0; b < 2; ++b)
; #pragma unroll
;                     for (int m = 0; m < 4; ++m)
; #pragma unroll
;                         for (int n = 0; n < 2; ++n) acc[a][b][m][n] = (f32x4){0.f, 0.f, 0.f, 0.f}; }
.LBB0_1919:
	s_ashr_i32 s15, s14, 31
	s_lshl_b64 s[16:17], s[14:15], 19
	s_add_u32 s16, s42, s16
	s_addc_u32 s17, s43, s17
	s_ashr_i32 s13, s12, 31
	s_lshl_b64 s[18:19], s[12:13], 19
	s_add_u32 s18, s8, s18
	v_mov_b32_e32 v4, 0
	s_addc_u32 s19, s44, s19
	s_mov_b32 s13, -2
	s_mov_b64 s[30:31], 0x40080
	v_mov_b32_e32 v5, v4
	v_mov_b32_e32 v6, v4
	v_mov_b32_e32 v7, v4
	v_mov_b32_e32 v8, v4
	v_mov_b32_e32 v9, v4
	v_mov_b32_e32 v10, v4
	v_mov_b32_e32 v11, v4
	v_mov_b32_e32 v20, v4
	v_mov_b32_e32 v21, v4
	v_mov_b32_e32 v22, v4
	v_mov_b32_e32 v23, v4
	v_mov_b32_e32 v24, v4
	v_mov_b32_e32 v25, v4
	v_mov_b32_e32 v26, v4
	v_mov_b32_e32 v27, v4
	v_mov_b32_e32 v36, v4
	v_mov_b32_e32 v37, v4
	v_mov_b32_e32 v38, v4
	v_mov_b32_e32 v39, v4
	v_mov_b32_e32 v40, v4
	v_mov_b32_e32 v41, v4
	v_mov_b32_e32 v42, v4
	v_mov_b32_e32 v43, v4
	v_mov_b32_e32 v52, v4
	v_mov_b32_e32 v53, v4
	v_mov_b32_e32 v54, v4
	v_mov_b32_e32 v55, v4
	v_mov_b32_e32 v56, v4
	v_mov_b32_e32 v57, v4
	v_mov_b32_e32 v58, v4
	v_mov_b32_e32 v59, v4
	v_mov_b32_e32 v12, v4
	v_mov_b32_e32 v13, v4
	v_mov_b32_e32 v14, v4
	v_mov_b32_e32 v15, v4
	v_mov_b32_e32 v16, v4
	v_mov_b32_e32 v17, v4
	v_mov_b32_e32 v18, v4
	v_mov_b32_e32 v19, v4
	v_mov_b32_e32 v28, v4
	v_mov_b32_e32 v29, v4
	v_mov_b32_e32 v30, v4
	v_mov_b32_e32 v31, v4
	v_mov_b32_e32 v32, v4
	v_mov_b32_e32 v33, v4
	v_mov_b32_e32 v34, v4
	v_mov_b32_e32 v35, v4
	v_mov_b32_e32 v44, v4
	v_mov_b32_e32 v45, v4
	v_mov_b32_e32 v46, v4
	v_mov_b32_e32 v47, v4
	v_mov_b32_e32 v48, v4
	v_mov_b32_e32 v49, v4
	v_mov_b32_e32 v50, v4
	v_mov_b32_e32 v51, v4
	v_mov_b32_e32 v60, v4
	v_mov_b32_e32 v61, v4
	v_mov_b32_e32 v62, v4
	v_mov_b32_e32 v63, v4
	v_mov_b32_e32 v64, v4
	v_mov_b32_e32 v65, v4
	v_mov_b32_e32 v66, v4
	v_mov_b32_e32 v67, v4
	v_mov_b32_e32 v68, v4
	v_mov_b32_e32 v69, v4
	v_mov_b32_e32 v70, v4
	v_mov_b32_e32 v71, v4
	v_mov_b32_e32 v72, v4
	v_mov_b32_e32 v73, v4
	v_mov_b32_e32 v74, v4
	v_mov_b32_e32 v75, v4
	v_mov_b32_e32 v84, v4
	v_mov_b32_e32 v85, v4
	v_mov_b32_e32 v86, v4
	v_mov_b32_e32 v87, v4
	v_mov_b32_e32 v88, v4
	v_mov_b32_e32 v89, v4
	v_mov_b32_e32 v90, v4
	v_mov_b32_e32 v91, v4
	v_mov_b32_e32 v100, v4
	v_mov_b32_e32 v101, v4
	v_mov_b32_e32 v102, v4
	v_mov_b32_e32 v103, v4
	v_mov_b32_e32 v104, v4
	v_mov_b32_e32 v105, v4
	v_mov_b32_e32 v106, v4
	v_mov_b32_e32 v107, v4
	v_mov_b32_e32 v116, v4
	v_mov_b32_e32 v117, v4
	v_mov_b32_e32 v118, v4
	v_mov_b32_e32 v119, v4
	v_mov_b32_e32 v120, v4
	v_mov_b32_e32 v121, v4
	v_mov_b32_e32 v122, v4
	v_mov_b32_e32 v123, v4
	v_mov_b32_e32 v76, v4
	v_mov_b32_e32 v77, v4
	v_mov_b32_e32 v78, v4
	v_mov_b32_e32 v79, v4
	v_mov_b32_e32 v80, v4
	v_mov_b32_e32 v81, v4
	v_mov_b32_e32 v82, v4
	v_mov_b32_e32 v83, v4
	v_mov_b32_e32 v92, v4
	v_mov_b32_e32 v93, v4
	v_mov_b32_e32 v94, v4
	v_mov_b32_e32 v95, v4
	v_mov_b32_e32 v96, v4
	v_mov_b32_e32 v97, v4
	v_mov_b32_e32 v98, v4
	v_mov_b32_e32 v99, v4
	v_mov_b32_e32 v108, v4
	v_mov_b32_e32 v109, v4
	v_mov_b32_e32 v110, v4
	v_mov_b32_e32 v111, v4
	v_mov_b32_e32 v112, v4
	v_mov_b32_e32 v113, v4
	v_mov_b32_e32 v114, v4
	v_mov_b32_e32 v115, v4
	v_mov_b32_e32 v124, v4
	v_mov_b32_e32 v125, v4
	v_mov_b32_e32 v126, v4
	v_mov_b32_e32 v127, v4
	v_mov_b32_e32 v128, v4
	v_mov_b32_e32 v129, v4
	v_mov_b32_e32 v130, v4
	v_mov_b32_e32 v131, v4
	v_add_u32_e32 v144, 0x10000, v159
	v_add_u32_e32 v149, 0x14000, v159
.LBB0_1920:
	ds_read_b128 v[132:135], v144
	ds_read_b128 v[136:139], v144 offset:1024
	ds_read_b128 v[140:143], v144 offset:2048
	ds_read_b128 v[144:147], v144 offset:3072
	ds_read_b128 v[154:157], v149
	ds_read_b128 v[162:165], v149 offset:1024
	ds_read_b128 v[166:169], v149 offset:2048
	ds_read_b128 v[170:173], v149 offset:3072
	ds_read_b128 v[174:177], v160
	ds_read_b128 v[178:181], v160 offset:1024
	ds_read_b128 v[182:185], v160 offset:2048
	ds_read_b128 v[186:189], v160 offset:3072
	ds_read_b128 v[190:193], v160 offset:4096
	ds_read_b128 v[194:197], v160 offset:5120
	ds_read_b128 v[198:201], v160 offset:6144
	ds_read_b128 v[202:205], v160 offset:7168
	s_add_u32 s15, s30, 0xfffc0080
	s_addc_u32 s21, s31, -1
	s_cmp_eq_u32 s13, 12
	s_cselect_b64 s[26:27], -1, 0
	s_and_b64 s[34:35], s[26:27], exec
	s_cselect_b32 s21, 0, s21
	s_cselect_b32 s15, 0, s15
	s_and_b64 s[26:27], s[26:27], s[36:37]
	s_and_b64 s[34:35], s[26:27], exec
	s_cselect_b32 s33, s18, s22
	s_cselect_b32 s28, s19, s23
	s_add_u32 s38, s33, s15
	s_addc_u32 s39, s28, s21
	s_add_i32 s28, 0, 0x10000
	s_and_b64 s[26:27], s[26:27], exec
	s_cselect_b32 s33, s17, s1
	s_cselect_b32 s34, s16, s0
	s_add_i32 s35, 0, 0x14000
	s_add_i32 m0, s48, 0xc000
	s_add_u32 s26, s0, s30
	s_addc_u32 s27, s1, s31
	global_load_lds_dwordx4 v2, s[26:27]
	s_add_i32 m0, s48, 0xe000
	v_mov_b32_e32 v151, v3
	global_load_lds_dwordx4 v150, s[26:27]
	s_waitcnt vmcnt(8)
	s_waitcnt lgkmcnt(0)
	s_barrier
	s_setprio 1
	s_waitcnt lgkmcnt(0)
	v_mfma_f32_16x16x32_bf16 v[128:131], v[132:135], v[174:177], v[128:131]
	v_mfma_f32_16x16x32_bf16 v[124:127], v[140:143], v[174:177], v[124:127]
	v_mfma_f32_16x16x32_bf16 v[112:115], v[132:135], v[182:185], v[112:115]
	v_mfma_f32_16x16x32_bf16 v[108:111], v[140:143], v[182:185], v[108:111]
	v_mfma_f32_16x16x32_bf16 v[96:99], v[132:135], v[190:193], v[96:99]
	v_mfma_f32_16x16x32_bf16 v[92:95], v[140:143], v[190:193], v[92:95]
	v_mfma_f32_16x16x32_bf16 v[80:83], v[132:135], v[198:201], v[80:83]
	v_mfma_f32_16x16x32_bf16 v[76:79], v[140:143], v[198:201], v[76:79]
	v_mfma_f32_16x16x32_bf16 v[128:131], v[136:139], v[178:181], v[128:131]
	v_mfma_f32_16x16x32_bf16 v[124:127], v[144:147], v[178:181], v[124:127]
	v_mfma_f32_16x16x32_bf16 v[112:115], v[136:139], v[186:189], v[112:115]
	v_mfma_f32_16x16x32_bf16 v[108:111], v[144:147], v[186:189], v[108:111]
	v_mfma_f32_16x16x32_bf16 v[96:99], v[136:139], v[194:197], v[96:99]
	v_mfma_f32_16x16x32_bf16 v[92:95], v[144:147], v[194:197], v[92:95]
	v_mfma_f32_16x16x32_bf16 v[80:83], v[136:139], v[202:205], v[80:83]
	v_mfma_f32_16x16x32_bf16 v[76:79], v[144:147], v[202:205], v[76:79]
	s_setprio 0
	s_setprio 1
	v_mfma_f32_16x16x32_bf16 v[120:123], v[154:157], v[174:177], v[120:123]
	v_mfma_f32_16x16x32_bf16 v[116:119], v[166:169], v[174:177], v[116:119]
	v_mfma_f32_16x16x32_bf16 v[104:107], v[154:157], v[182:185], v[104:107]
	v_mfma_f32_16x16x32_bf16 v[100:103], v[166:169], v[182:185], v[100:103]
	v_mfma_f32_16x16x32_bf16 v[88:91], v[154:157], v[190:193], v[88:91]
	v_mfma_f32_16x16x32_bf16 v[84:87], v[166:169], v[190:193], v[84:87]
	v_mfma_f32_16x16x32_bf16 v[72:75], v[154:157], v[198:201], v[72:75]
	v_mfma_f32_16x16x32_bf16 v[68:71], v[166:169], v[198:201], v[68:71]
	v_mfma_f32_16x16x32_bf16 v[120:123], v[162:165], v[178:181], v[120:123]
	v_mfma_f32_16x16x32_bf16 v[116:119], v[170:173], v[178:181], v[116:119]
	v_mfma_f32_16x16x32_bf16 v[104:107], v[162:165], v[186:189], v[104:107]
	v_mfma_f32_16x16x32_bf16 v[100:103], v[170:173], v[186:189], v[100:103]
	v_mfma_f32_16x16x32_bf16 v[88:91], v[162:165], v[194:197], v[88:91]
	v_mfma_f32_16x16x32_bf16 v[84:87], v[170:173], v[194:197], v[84:87]
	v_mfma_f32_16x16x32_bf16 v[72:75], v[162:165], v[202:205], v[72:75]
	v_mfma_f32_16x16x32_bf16 v[68:71], v[170:173], v[202:205], v[68:71]
	s_setprio 0
	s_barrier
	ds_read_b128 v[174:177], v160 offset:16384
	ds_read_b128 v[178:181], v160 offset:17408
	ds_read_b128 v[182:185], v160 offset:18432
	ds_read_b128 v[186:189], v160 offset:19456
	ds_read_b128 v[190:193], v160 offset:20480
	ds_read_b128 v[194:197], v160 offset:21504
	ds_read_b128 v[198:201], v160 offset:22528
	ds_read_b128 v[202:205], v160 offset:23552
	s_add_i32 s26, s28, s45
	s_mov_b32 m0, s26
	global_load_lds_dwordx4 v148, s[38:39]
	s_add_i32 m0, s26, 0x2000
	s_add_u32 s26, s38, 0x40000
	s_addc_u32 s27, s39, 0
	s_add_i32 s28, s35, s45
	global_load_lds_dwordx4 v152, s[38:39]
	s_mov_b32 m0, s28
	v_mov_b32_e32 v149, v3
	global_load_lds_dwordx4 v148, s[26:27]
	s_add_i32 m0, s28, 0x2000
	v_mov_b32_e32 v153, v3
	global_load_lds_dwordx4 v152, s[26:27]
	s_add_u32 s26, s34, s15
	s_addc_u32 s27, s33, s21
	s_mov_b32 m0, s48
	v_lshl_add_u64 v[206:207], s[38:39], 0, v[148:149]
	global_load_lds_dwordx4 v2, s[26:27]
	s_mov_b32 m0, s49
	v_lshl_add_u64 v[208:209], s[38:39], 0, v[152:153]
	global_load_lds_dwordx4 v150, s[26:27]
	s_waitcnt vmcnt(8)
	s_waitcnt lgkmcnt(0)
	v_lshl_add_u64 v[210:211], s[26:27], 0, v[2:3]
	v_lshl_add_u64 v[212:213], s[26:27], 0, v[150:151]
	s_barrier
	s_setprio 1
	s_waitcnt lgkmcnt(0)
	v_mfma_f32_16x16x32_bf16 v[64:67], v[132:135], v[174:177], v[64:67]
	v_mfma_f32_16x16x32_bf16 v[60:63], v[140:143], v[174:177], v[60:63]
	v_mfma_f32_16x16x32_bf16 v[48:51], v[132:135], v[182:185], v[48:51]
	v_mfma_f32_16x16x32_bf16 v[44:47], v[140:143], v[182:185], v[44:47]
	v_mfma_f32_16x16x32_bf16 v[32:35], v[132:135], v[190:193], v[32:35]
	v_mfma_f32_16x16x32_bf16 v[28:31], v[140:143], v[190:193], v[28:31]
	v_mfma_f32_16x16x32_bf16 v[16:19], v[132:135], v[198:201], v[16:19]
	v_mfma_f32_16x16x32_bf16 v[12:15], v[140:143], v[198:201], v[12:15]
	v_mfma_f32_16x16x32_bf16 v[64:67], v[136:139], v[178:181], v[64:67]
	v_mfma_f32_16x16x32_bf16 v[60:63], v[144:147], v[178:181], v[60:63]
	v_mfma_f32_16x16x32_bf16 v[48:51], v[136:139], v[186:189], v[48:51]
	v_mfma_f32_16x16x32_bf16 v[44:47], v[144:147], v[186:189], v[44:47]
	v_mfma_f32_16x16x32_bf16 v[32:35], v[136:139], v[194:197], v[32:35]
	v_mfma_f32_16x16x32_bf16 v[28:31], v[144:147], v[194:197], v[28:31]
	v_mfma_f32_16x16x32_bf16 v[16:19], v[136:139], v[202:205], v[16:19]
	v_mfma_f32_16x16x32_bf16 v[12:15], v[144:147], v[202:205], v[12:15]
	s_setprio 0
	s_setprio 1
	v_mfma_f32_16x16x32_bf16 v[56:59], v[154:157], v[174:177], v[56:59]
	v_mfma_f32_16x16x32_bf16 v[52:55], v[166:169], v[174:177], v[52:55]
	v_mfma_f32_16x16x32_bf16 v[40:43], v[154:157], v[182:185], v[40:43]
	v_mfma_f32_16x16x32_bf16 v[36:39], v[166:169], v[182:185], v[36:39]
	v_mfma_f32_16x16x32_bf16 v[24:27], v[154:157], v[190:193], v[24:27]
	v_mfma_f32_16x16x32_bf16 v[20:23], v[166:169], v[190:193], v[20:23]
	v_mfma_f32_16x16x32_bf16 v[8:11], v[154:157], v[198:201], v[8:11]
	v_mfma_f32_16x16x32_bf16 v[4:7], v[166:169], v[198:201], v[4:7]
	v_mfma_f32_16x16x32_bf16 v[56:59], v[162:165], v[178:181], v[56:59]
	v_mfma_f32_16x16x32_bf16 v[52:55], v[170:173], v[178:181], v[52:55]
	v_mfma_f32_16x16x32_bf16 v[40:43], v[162:165], v[186:189], v[40:43]
	v_mfma_f32_16x16x32_bf16 v[36:39], v[170:173], v[186:189], v[36:39]
	v_mfma_f32_16x16x32_bf16 v[24:27], v[162:165], v[194:197], v[24:27]
	v_mfma_f32_16x16x32_bf16 v[20:23], v[170:173], v[194:197], v[20:23]
	v_mfma_f32_16x16x32_bf16 v[8:11], v[162:165], v[202:205], v[8:11]
	v_mfma_f32_16x16x32_bf16 v[4:7], v[170:173], v[202:205], v[4:7]
	v_add_u32_e32 v144, 0x18000, v159
	v_add_u32_e32 v149, 0x1c000, v159
	s_setprio 0
	s_barrier
; template <class P, bool ALIGN_EPI>
; __device__ __forceinline__ void gemm_phase(ldsp lds, ldsp tab, const P& S) {
;     ...
;             for (int t = 2; t < nt; t += 2) PG8_TRIP(t, PG8_MMA);
;         } else {
;             for (int t = 0; t < nt; t += 2) PG8_TRIP(t, PG8_MMA);
	ds_read_b128 v[132:135], v144
	ds_read_b128 v[136:139], v144 offset:1024
	ds_read_b128 v[140:143], v144 offset:2048
	ds_read_b128 v[144:147], v144 offset:3072
	ds_read_b128 v[154:157], v149
	ds_read_b128 v[162:165], v149 offset:1024
	ds_read_b128 v[166:169], v149 offset:2048
	ds_read_b128 v[170:173], v149 offset:3072
	ds_read_b128 v[174:177], v160 offset:32768
	ds_read_b128 v[178:181], v160 offset:33792
	ds_read_b128 v[182:185], v160 offset:34816
	ds_read_b128 v[186:189], v160 offset:35840
	ds_read_b128 v[190:193], v160 offset:36864
	ds_read_b128 v[194:197], v160 offset:37888
	ds_read_b128 v[198:201], v160 offset:38912
	ds_read_b128 v[202:205], v160 offset:39936
	s_add_i32 s15, 0, 0x18000
	s_add_i32 s21, 0, 0x1c000
	s_add_u32 s26, s26, 0x40000
	s_addc_u32 s27, s27, 0
	s_mov_b32 m0, s50
	global_load_lds_dwordx4 v2, s[26:27]
	s_mov_b32 m0, s51
	s_nop 0
	global_load_lds_dwordx4 v150, s[26:27]
	s_waitcnt vmcnt(8)
	s_waitcnt lgkmcnt(0)
	s_barrier
	s_setprio 1
	s_waitcnt lgkmcnt(0)
	v_mfma_f32_16x16x32_bf16 v[128:131], v[132:135], v[174:177], v[128:131]
	v_mfma_f32_16x16x32_bf16 v[124:127], v[140:143], v[174:177], v[124:127]
	v_mfma_f32_16x16x32_bf16 v[112:115], v[132:135], v[182:185], v[112:115]
	v_mfma_f32_16x16x32_bf16 v[108:111], v[140:143], v[182:185], v[108:111]
	v_mfma_f32_16x16x32_bf16 v[96:99], v[132:135], v[190:193], v[96:99]
	v_mfma_f32_16x16x32_bf16 v[92:95], v[140:143], v[190:193], v[92:95]
	v_mfma_f32_16x16x32_bf16 v[80:83], v[132:135], v[198:201], v[80:83]
	v_mfma_f32_16x16x32_bf16 v[76:79], v[140:143], v[198:201], v[76:79]
	v_mfma_f32_16x16x32_bf16 v[128:131], v[136:139], v[178:181], v[128:131]
	v_mfma_f32_16x16x32_bf16 v[124:127], v[144:147], v[178:181], v[124:127]
	v_mfma_f32_16x16x32_bf16 v[112:115], v[136:139], v[186:189], v[112:115]
	v_mfma_f32_16x16x32_bf16 v[108:111], v[144:147], v[186:189], v[108:111]
	v_mfma_f32_16x16x32_bf16 v[96:99], v[136:139], v[194:197], v[96:99]
	v_mfma_f32_16x16x32_bf16 v[92:95], v[144:147], v[194:197], v[92:95]
	v_mfma_f32_16x16x32_bf16 v[80:83], v[136:139], v[202:205], v[80:83]
	v_mfma_f32_16x16x32_bf16 v[76:79], v[144:147], v[202:205], v[76:79]
	s_setprio 0
	s_setprio 1
	v_mfma_f32_16x16x32_bf16 v[120:123], v[154:157], v[174:177], v[120:123]
	v_mfma_f32_16x16x32_bf16 v[116:119], v[166:169], v[174:177], v[116:119]
	v_mfma_f32_16x16x32_bf16 v[104:107], v[154:157], v[182:185], v[104:107]
	v_mfma_f32_16x16x32_bf16 v[100:103], v[166:169], v[182:185], v[100:103]
	v_mfma_f32_16x16x32_bf16 v[88:91], v[154:157], v[190:193], v[88:91]
	v_mfma_f32_16x16x32_bf16 v[84:87], v[166:169], v[190:193], v[84:87]
	v_mfma_f32_16x16x32_bf16 v[72:75], v[154:157], v[198:201], v[72:75]
	v_mfma_f32_16x16x32_bf16 v[68:71], v[166:169], v[198:201], v[68:71]
	v_mfma_f32_16x16x32_bf16 v[120:123], v[162:165], v[178:181], v[120:123]
	v_mfma_f32_16x16x32_bf16 v[116:119], v[170:173], v[178:181], v[116:119]
	v_mfma_f32_16x16x32_bf16 v[104:107], v[162:165], v[186:189], v[104:107]
	v_mfma_f32_16x16x32_bf16 v[100:103], v[170:173], v[186:189], v[100:103]
	v_mfma_f32_16x16x32_bf16 v[88:91], v[162:165], v[194:197], v[88:91]
	v_mfma_f32_16x16x32_bf16 v[84:87], v[170:173], v[194:197], v[84:87]
	v_mfma_f32_16x16x32_bf16 v[72:75], v[162:165], v[202:205], v[72:75]
	v_mfma_f32_16x16x32_bf16 v[68:71], v[170:173], v[202:205], v[68:71]
	s_setprio 0
	s_barrier
	ds_read_b128 v[174:177], v160 offset:49152
	ds_read_b128 v[178:181], v160 offset:50176
	ds_read_b128 v[182:185], v160 offset:51200
	ds_read_b128 v[186:189], v160 offset:52224
	ds_read_b128 v[190:193], v160 offset:53248
	ds_read_b128 v[194:197], v160 offset:54272
	ds_read_b128 v[198:201], v160 offset:55296
	ds_read_b128 v[202:205], v160 offset:56320
	s_add_i32 s15, s15, s45
	v_lshl_add_u64 v[206:207], v[206:207], 0, s[24:25]
	s_mov_b32 m0, s15
	global_load_lds_dwordx4 v[206:207], off
	s_add_i32 m0, s15, 0x2000
	s_add_u32 s26, s38, 0x40080
	v_lshl_add_u64 v[206:207], v[208:209], 0, s[24:25]
	s_addc_u32 s27, s39, 0
	s_add_i32 s15, s21, s45
	global_load_lds_dwordx4 v[206:207], off
	s_mov_b32 m0, s15
	v_lshl_add_u64 v[206:207], v[210:211], 0, s[24:25]
	global_load_lds_dwordx4 v148, s[26:27]
	s_add_i32 m0, s15, 0x2000
	s_nop 0
	global_load_lds_dwordx4 v152, s[26:27]
	s_mov_b32 m0, s53
	s_nop 0
	global_load_lds_dwordx4 v[206:207], off
	v_lshl_add_u64 v[206:207], v[212:213], 0, s[24:25]
	s_mov_b32 m0, s54
	s_nop 0
	global_load_lds_dwordx4 v[206:207], off
	s_waitcnt vmcnt(8)
	s_waitcnt lgkmcnt(0)
	s_barrier
	s_setprio 1
	s_waitcnt lgkmcnt(0)
	v_mfma_f32_16x16x32_bf16 v[64:67], v[132:135], v[174:177], v[64:67]
	v_mfma_f32_16x16x32_bf16 v[60:63], v[140:143], v[174:177], v[60:63]
	v_mfma_f32_16x16x32_bf16 v[48:51], v[132:135], v[182:185], v[48:51]
	v_mfma_f32_16x16x32_bf16 v[44:47], v[140:143], v[182:185], v[44:47]
	v_mfma_f32_16x16x32_bf16 v[32:35], v[132:135], v[190:193], v[32:35]
	v_mfma_f32_16x16x32_bf16 v[28:31], v[140:143], v[190:193], v[28:31]
	v_mfma_f32_16x16x32_bf16 v[16:19], v[132:135], v[198:201], v[16:19]
	v_mfma_f32_16x16x32_bf16 v[12:15], v[140:143], v[198:201], v[12:15]
	v_mfma_f32_16x16x32_bf16 v[64:67], v[136:139], v[178:181], v[64:67]
	v_mfma_f32_16x16x32_bf16 v[60:63], v[144:147], v[178:181], v[60:63]
	v_mfma_f32_16x16x32_bf16 v[48:51], v[136:139], v[186:189], v[48:51]
	v_mfma_f32_16x16x32_bf16 v[44:47], v[144:147], v[186:189], v[44:47]
	v_mfma_f32_16x16x32_bf16 v[32:35], v[136:139], v[194:197], v[32:35]
	v_mfma_f32_16x16x32_bf16 v[28:31], v[144:147], v[194:197], v[28:31]
	v_mfma_f32_16x16x32_bf16 v[16:19], v[136:139], v[202:205], v[16:19]
	v_mfma_f32_16x16x32_bf16 v[12:15], v[144:147], v[202:205], v[12:15]
	s_setprio 0
	s_setprio 1
	v_mfma_f32_16x16x32_bf16 v[56:59], v[154:157], v[174:177], v[56:59]
	v_mfma_f32_16x16x32_bf16 v[52:55], v[166:169], v[174:177], v[52:55]
	v_mfma_f32_16x16x32_bf16 v[40:43], v[154:157], v[182:185], v[40:43]
	v_mfma_f32_16x16x32_bf16 v[36:39], v[166:169], v[182:185], v[36:39]
	v_mfma_f32_16x16x32_bf16 v[24:27], v[154:157], v[190:193], v[24:27]
	v_mfma_f32_16x16x32_bf16 v[20:23], v[166:169], v[190:193], v[20:23]
	v_mfma_f32_16x16x32_bf16 v[8:11], v[154:157], v[198:201], v[8:11]
	v_mfma_f32_16x16x32_bf16 v[4:7], v[166:169], v[198:201], v[4:7]
	v_mfma_f32_16x16x32_bf16 v[56:59], v[162:165], v[178:181], v[56:59]
	v_mfma_f32_16x16x32_bf16 v[52:55], v[170:173], v[178:181], v[52:55]
	v_mfma_f32_16x16x32_bf16 v[40:43], v[162:165], v[186:189], v[40:43]
	v_mfma_f32_16x16x32_bf16 v[36:39], v[170:173], v[186:189], v[36:39]
	v_mfma_f32_16x16x32_bf16 v[24:27], v[162:165], v[194:197], v[24:27]
	v_mfma_f32_16x16x32_bf16 v[20:23], v[170:173], v[194:197], v[20:23]
	v_mfma_f32_16x16x32_bf16 v[8:11], v[162:165], v[202:205], v[8:11]
	v_mfma_f32_16x16x32_bf16 v[4:7], v[170:173], v[202:205], v[4:7]
	v_add_u32_e32 v144, 0x10000, v159
	v_add_u32_e32 v149, 0x14000, v159
	s_setprio 0
	s_barrier
	s_add_i32 s13, s13, 2
	s_add_u32 s30, s30, 0x100
	s_addc_u32 s31, s31, 0
	s_cmp_gt_u32 s13, 13
	s_cbranch_scc0 .LBB0_1920
	s_and_b64 vcc, exec, s[10:11]
	s_cbranch_vccz .LBB0_1923
	s_barrier

; template <class P, bool ALIGN_EPI>
; __device__ __forceinline__ void gemm_phase(ldsp lds, ldsp tab, const P& S) {
;     ...
;         if constexpr (!P::FP8) {
; #pragma unroll
;             for (int a = 0; a < 2; ++a)
; #pragma unroll
;                 for (int b = 0; b < 2; ++b)
; #pragma unroll
;                     for (int m = 0; m < 4; ++m)
; #pragma unroll
;                         for (int n = 0; n < 2; ++n) acc[a][b][m][n] = (f32x4){0.f, 0.f, 0.f, 0.f}; }
.LBB0_2006:
	v_mov_b32_e32 v4, 0
	s_mov_b32 s2, -2
	s_mov_b64 s[22:23], 0xa0080
	v_mov_b32_e32 v5, v4
	v_mov_b32_e32 v6, v4
	v_mov_b32_e32 v7, v4
	v_mov_b32_e32 v8, v4
	v_mov_b32_e32 v9, v4
	v_mov_b32_e32 v10, v4
	v_mov_b32_e32 v11, v4
	v_mov_b32_e32 v12, v4
	v_mov_b32_e32 v13, v4
	v_mov_b32_e32 v14, v4
	v_mov_b32_e32 v15, v4
	v_mov_b32_e32 v16, v4
	v_mov_b32_e32 v17, v4
	v_mov_b32_e32 v18, v4
	v_mov_b32_e32 v19, v4
	v_mov_b32_e32 v20, v4
	v_mov_b32_e32 v21, v4
	v_mov_b32_e32 v22, v4
	v_mov_b32_e32 v23, v4
	v_mov_b32_e32 v24, v4
	v_mov_b32_e32 v25, v4
	v_mov_b32_e32 v26, v4
	v_mov_b32_e32 v27, v4
	v_mov_b32_e32 v28, v4
	v_mov_b32_e32 v29, v4
	v_mov_b32_e32 v30, v4
	v_mov_b32_e32 v31, v4
	v_mov_b32_e32 v32, v4
	v_mov_b32_e32 v33, v4
	v_mov_b32_e32 v34, v4
	v_mov_b32_e32 v35, v4
	v_mov_b32_e32 v64, v4
	v_mov_b32_e32 v65, v4
	v_mov_b32_e32 v66, v4
	v_mov_b32_e32 v67, v4
	v_mov_b32_e32 v72, v4
	v_mov_b32_e32 v73, v4
	v_mov_b32_e32 v74, v4
	v_mov_b32_e32 v75, v4
	v_mov_b32_e32 v76, v4
	v_mov_b32_e32 v77, v4
	v_mov_b32_e32 v78, v4
	v_mov_b32_e32 v79, v4
	v_mov_b32_e32 v80, v4
	v_mov_b32_e32 v81, v4
	v_mov_b32_e32 v82, v4
	v_mov_b32_e32 v83, v4
	v_mov_b32_e32 v84, v4
	v_mov_b32_e32 v85, v4
	v_mov_b32_e32 v86, v4
	v_mov_b32_e32 v87, v4
	v_mov_b32_e32 v88, v4
	v_mov_b32_e32 v89, v4
	v_mov_b32_e32 v90, v4
	v_mov_b32_e32 v91, v4
	v_mov_b32_e32 v92, v4
	v_mov_b32_e32 v93, v4
	v_mov_b32_e32 v94, v4
	v_mov_b32_e32 v95, v4
	v_mov_b32_e32 v96, v4
	v_mov_b32_e32 v97, v4
	v_mov_b32_e32 v98, v4
	v_mov_b32_e32 v99, v4
	v_mov_b32_e32 v36, v4
	v_mov_b32_e32 v37, v4
	v_mov_b32_e32 v38, v4
	v_mov_b32_e32 v39, v4
	v_mov_b32_e32 v40, v4
	v_mov_b32_e32 v41, v4
	v_mov_b32_e32 v42, v4
	v_mov_b32_e32 v43, v4
	v_mov_b32_e32 v44, v4
	v_mov_b32_e32 v45, v4
	v_mov_b32_e32 v46, v4
	v_mov_b32_e32 v47, v4
	v_mov_b32_e32 v48, v4
	v_mov_b32_e32 v49, v4
	v_mov_b32_e32 v50, v4
	v_mov_b32_e32 v51, v4
	v_mov_b32_e32 v52, v4
	v_mov_b32_e32 v53, v4
	v_mov_b32_e32 v54, v4
	v_mov_b32_e32 v55, v4
	v_mov_b32_e32 v56, v4
	v_mov_b32_e32 v57, v4
	v_mov_b32_e32 v58, v4
	v_mov_b32_e32 v59, v4
	v_mov_b32_e32 v60, v4
	v_mov_b32_e32 v61, v4
	v_mov_b32_e32 v62, v4
	v_mov_b32_e32 v63, v4
	v_mov_b32_e32 v68, v4
	v_mov_b32_e32 v69, v4
	v_mov_b32_e32 v70, v4
	v_mov_b32_e32 v71, v4
	v_mov_b32_e32 v116, v4
	v_mov_b32_e32 v117, v4
	v_mov_b32_e32 v118, v4
	v_mov_b32_e32 v119, v4
	v_mov_b32_e32 v120, v4
	v_mov_b32_e32 v121, v4
	v_mov_b32_e32 v122, v4
	v_mov_b32_e32 v123, v4
	v_mov_b32_e32 v124, v4
	v_mov_b32_e32 v125, v4
	v_mov_b32_e32 v126, v4
	v_mov_b32_e32 v127, v4
	v_mov_b32_e32 v128, v4
	v_mov_b32_e32 v129, v4
	v_mov_b32_e32 v130, v4
	v_mov_b32_e32 v131, v4
	v_mov_b32_e32 v132, v4
	v_mov_b32_e32 v133, v4
	v_mov_b32_e32 v134, v4
	v_mov_b32_e32 v135, v4
	v_mov_b32_e32 v136, v4
	v_mov_b32_e32 v137, v4
	v_mov_b32_e32 v138, v4
	v_mov_b32_e32 v139, v4
	v_mov_b32_e32 v140, v4
	v_mov_b32_e32 v141, v4
	v_mov_b32_e32 v142, v4
	v_mov_b32_e32 v143, v4
	v_mov_b32_e32 v144, v4
	v_mov_b32_e32 v145, v4
	v_mov_b32_e32 v146, v4
	v_mov_b32_e32 v147, v4
	v_add_u32_e32 v112, 0x10000, v239
	v_add_u32_e32 v160, 0x14000, v239
.LBB0_2007:
	ds_read_b128 v[100:103], v112
	ds_read_b128 v[104:107], v112 offset:1024
	ds_read_b128 v[108:111], v112 offset:2048
	ds_read_b128 v[112:115], v112 offset:3072
	ds_read_b128 v[148:151], v160
	ds_read_b128 v[152:155], v160 offset:1024
	ds_read_b128 v[156:159], v160 offset:2048
	ds_read_b128 v[160:163], v160 offset:3072
	ds_read_b128 v[164:167], v249
	ds_read_b128 v[168:171], v249 offset:1024
	ds_read_b128 v[172:175], v249 offset:2048
	ds_read_b128 v[176:179], v249 offset:3072
	ds_read_b128 v[180:183], v249 offset:4096
	ds_read_b128 v[190:193], v249 offset:5120
	ds_read_b128 v[194:197], v249 offset:6144
	ds_read_b128 v[198:201], v249 offset:7168
	s_add_u32 s3, s22, 0xfff60080
	s_addc_u32 s15, s23, -1
	s_cmp_eq_u32 s2, 36
	s_cselect_b32 s27, s16, s18
	s_cselect_b32 s3, 0, s3
	s_cselect_b32 s26, s17, s19
	s_cselect_b32 s15, 0, s15
	s_cselect_b32 s28, s0, s20
	s_cselect_b32 s33, s1, s21
	s_add_u32 s30, s27, s3
	s_addc_u32 s31, s26, s15
	s_add_i32 s34, 0, 0x10000
	s_add_i32 s35, 0, 0x14000
	s_add_i32 m0, s43, 0xc000
	s_add_u32 s26, s20, s22
	s_addc_u32 s27, s21, s23
	global_load_lds_dwordx4 v2, s[26:27]
	s_add_i32 m0, s43, 0xe000
	v_mov_b32_e32 v187, v3
	global_load_lds_dwordx4 v186, s[26:27]
	s_waitcnt vmcnt(8)
	s_waitcnt lgkmcnt(0)
	s_barrier
	s_setprio 1
	s_waitcnt lgkmcnt(0)
	v_mfma_f32_16x16x32_bf16 v[144:147], v[100:103], v[164:167], v[144:147]
	v_mfma_f32_16x16x32_bf16 v[140:143], v[108:111], v[164:167], v[140:143]
	v_mfma_f32_16x16x32_bf16 v[136:139], v[100:103], v[172:175], v[136:139]
	v_mfma_f32_16x16x32_bf16 v[132:135], v[108:111], v[172:175], v[132:135]
	v_mfma_f32_16x16x32_bf16 v[128:131], v[100:103], v[180:183], v[128:131]
	v_mfma_f32_16x16x32_bf16 v[124:127], v[108:111], v[180:183], v[124:127]
	v_mfma_f32_16x16x32_bf16 v[120:123], v[100:103], v[194:197], v[120:123]
	v_mfma_f32_16x16x32_bf16 v[116:119], v[108:111], v[194:197], v[116:119]
	v_mfma_f32_16x16x32_bf16 v[144:147], v[104:107], v[168:171], v[144:147]
	v_mfma_f32_16x16x32_bf16 v[140:143], v[112:115], v[168:171], v[140:143]
	v_mfma_f32_16x16x32_bf16 v[136:139], v[104:107], v[176:179], v[136:139]
	v_mfma_f32_16x16x32_bf16 v[132:135], v[112:115], v[176:179], v[132:135]
	v_mfma_f32_16x16x32_bf16 v[128:131], v[104:107], v[190:193], v[128:131]
	v_mfma_f32_16x16x32_bf16 v[124:127], v[112:115], v[190:193], v[124:127]
	v_mfma_f32_16x16x32_bf16 v[120:123], v[104:107], v[198:201], v[120:123]
	v_mfma_f32_16x16x32_bf16 v[116:119], v[112:115], v[198:201], v[116:119]
	s_setprio 0
	s_setprio 1
	v_mfma_f32_16x16x32_bf16 v[68:71], v[148:151], v[164:167], v[68:71]
	v_mfma_f32_16x16x32_bf16 v[60:63], v[156:159], v[164:167], v[60:63]
	v_mfma_f32_16x16x32_bf16 v[56:59], v[148:151], v[172:175], v[56:59]
	v_mfma_f32_16x16x32_bf16 v[52:55], v[156:159], v[172:175], v[52:55]
	v_mfma_f32_16x16x32_bf16 v[48:51], v[148:151], v[180:183], v[48:51]
	v_mfma_f32_16x16x32_bf16 v[44:47], v[156:159], v[180:183], v[44:47]
	v_mfma_f32_16x16x32_bf16 v[40:43], v[148:151], v[194:197], v[40:43]
	v_mfma_f32_16x16x32_bf16 v[36:39], v[156:159], v[194:197], v[36:39]
	v_mfma_f32_16x16x32_bf16 v[68:71], v[152:155], v[168:171], v[68:71]
	v_mfma_f32_16x16x32_bf16 v[60:63], v[160:163], v[168:171], v[60:63]
	v_mfma_f32_16x16x32_bf16 v[56:59], v[152:155], v[176:179], v[56:59]
	v_mfma_f32_16x16x32_bf16 v[52:55], v[160:163], v[176:179], v[52:55]
	v_mfma_f32_16x16x32_bf16 v[48:51], v[152:155], v[190:193], v[48:51]
	v_mfma_f32_16x16x32_bf16 v[44:47], v[160:163], v[190:193], v[44:47]
	v_mfma_f32_16x16x32_bf16 v[40:43], v[152:155], v[198:201], v[40:43]
	v_mfma_f32_16x16x32_bf16 v[36:39], v[160:163], v[198:201], v[36:39]
	s_setprio 0
	s_barrier
	ds_read_b128 v[164:167], v249 offset:16384
	ds_read_b128 v[168:171], v249 offset:17408
	ds_read_b128 v[172:175], v249 offset:18432
	ds_read_b128 v[176:179], v249 offset:19456
	ds_read_b128 v[180:183], v249 offset:20480
	ds_read_b128 v[190:193], v249 offset:21504
	ds_read_b128 v[194:197], v249 offset:22528
	ds_read_b128 v[198:201], v249 offset:23552
	s_add_i32 s26, s34, s42
	s_mov_b32 m0, s26
	global_load_lds_dwordx4 v184, s[30:31]
	s_add_i32 m0, s26, 0x2000
	s_add_u32 s26, s30, 0xa0000
	s_addc_u32 s27, s31, 0
	s_add_i32 s34, s35, s42
	global_load_lds_dwordx4 v188, s[30:31]
	s_mov_b32 m0, s34
	v_mov_b32_e32 v185, v3
	global_load_lds_dwordx4 v184, s[26:27]
	s_add_i32 m0, s34, 0x2000
	v_mov_b32_e32 v189, v3
	global_load_lds_dwordx4 v188, s[26:27]
	s_add_u32 s26, s28, s3
	s_addc_u32 s27, s33, s15
	s_mov_b32 m0, s43
	v_lshl_add_u64 v[202:203], s[30:31], 0, v[184:185]
	global_load_lds_dwordx4 v2, s[26:27]
	s_mov_b32 m0, s44
	v_lshl_add_u64 v[204:205], s[30:31], 0, v[188:189]
	global_load_lds_dwordx4 v186, s[26:27]
	s_waitcnt vmcnt(8)
	s_waitcnt lgkmcnt(0)
	v_lshl_add_u64 v[206:207], s[26:27], 0, v[2:3]
	v_lshl_add_u64 v[208:209], s[26:27], 0, v[186:187]
	s_barrier
	s_setprio 1
	s_waitcnt lgkmcnt(0)
	v_mfma_f32_16x16x32_bf16 v[96:99], v[100:103], v[164:167], v[96:99]
	v_mfma_f32_16x16x32_bf16 v[92:95], v[108:111], v[164:167], v[92:95]
	v_mfma_f32_16x16x32_bf16 v[88:91], v[100:103], v[172:175], v[88:91]
	v_mfma_f32_16x16x32_bf16 v[84:87], v[108:111], v[172:175], v[84:87]
	v_mfma_f32_16x16x32_bf16 v[80:83], v[100:103], v[180:183], v[80:83]
	v_mfma_f32_16x16x32_bf16 v[76:79], v[108:111], v[180:183], v[76:79]
	v_mfma_f32_16x16x32_bf16 v[72:75], v[100:103], v[194:197], v[72:75]
	v_mfma_f32_16x16x32_bf16 v[64:67], v[108:111], v[194:197], v[64:67]
	v_mfma_f32_16x16x32_bf16 v[96:99], v[104:107], v[168:171], v[96:99]
	v_mfma_f32_16x16x32_bf16 v[92:95], v[112:115], v[168:171], v[92:95]
	v_mfma_f32_16x16x32_bf16 v[88:91], v[104:107], v[176:179], v[88:91]
	v_mfma_f32_16x16x32_bf16 v[84:87], v[112:115], v[176:179], v[84:87]
	v_mfma_f32_16x16x32_bf16 v[80:83], v[104:107], v[190:193], v[80:83]
	v_mfma_f32_16x16x32_bf16 v[76:79], v[112:115], v[190:193], v[76:79]
	v_mfma_f32_16x16x32_bf16 v[72:75], v[104:107], v[198:201], v[72:75]
	v_mfma_f32_16x16x32_bf16 v[64:67], v[112:115], v[198:201], v[64:67]
	s_setprio 0
	s_setprio 1
	v_mfma_f32_16x16x32_bf16 v[32:35], v[148:151], v[164:167], v[32:35]
	v_mfma_f32_16x16x32_bf16 v[28:31], v[156:159], v[164:167], v[28:31]
	v_mfma_f32_16x16x32_bf16 v[24:27], v[148:151], v[172:175], v[24:27]
	v_mfma_f32_16x16x32_bf16 v[20:23], v[156:159], v[172:175], v[20:23]
	v_mfma_f32_16x16x32_bf16 v[16:19], v[148:151], v[180:183], v[16:19]
	v_mfma_f32_16x16x32_bf16 v[12:15], v[156:159], v[180:183], v[12:15]
	v_mfma_f32_16x16x32_bf16 v[8:11], v[148:151], v[194:197], v[8:11]
	v_mfma_f32_16x16x32_bf16 v[4:7], v[156:159], v[194:197], v[4:7]
	v_mfma_f32_16x16x32_bf16 v[32:35], v[152:155], v[168:171], v[32:35]
	v_mfma_f32_16x16x32_bf16 v[28:31], v[160:163], v[168:171], v[28:31]
	v_mfma_f32_16x16x32_bf16 v[24:27], v[152:155], v[176:179], v[24:27]
	v_mfma_f32_16x16x32_bf16 v[20:23], v[160:163], v[176:179], v[20:23]
	v_mfma_f32_16x16x32_bf16 v[16:19], v[152:155], v[190:193], v[16:19]
	v_mfma_f32_16x16x32_bf16 v[12:15], v[160:163], v[190:193], v[12:15]
	v_mfma_f32_16x16x32_bf16 v[8:11], v[152:155], v[198:201], v[8:11]
	v_mfma_f32_16x16x32_bf16 v[4:7], v[160:163], v[198:201], v[4:7]
	v_add_u32_e32 v112, 0x18000, v239
	v_add_u32_e32 v160, 0x1c000, v239
	s_setprio 0
	s_barrier
	ds_read_b128 v[100:103], v112
	ds_read_b128 v[104:107], v112 offset:1024
	ds_read_b128 v[108:111], v112 offset:2048
	ds_read_b128 v[112:115], v112 offset:3072
	ds_read_b128 v[148:151], v160
	ds_read_b128 v[152:155], v160 offset:1024
	ds_read_b128 v[156:159], v160 offset:2048
	ds_read_b128 v[160:163], v160 offset:3072
	ds_read_b128 v[164:167], v249 offset:32768
	ds_read_b128 v[168:171], v249 offset:33792
	ds_read_b128 v[172:175], v249 offset:34816
	ds_read_b128 v[176:179], v249 offset:35840
	ds_read_b128 v[180:183], v249 offset:36864
	ds_read_b128 v[190:193], v249 offset:37888
	ds_read_b128 v[194:197], v249 offset:38912
	ds_read_b128 v[198:201], v249 offset:39936
	s_add_i32 s3, 0, 0x18000
	s_add_i32 s15, 0, 0x1c000
	s_add_u32 s26, s26, 0xa0000
	s_addc_u32 s27, s27, 0
	s_mov_b32 m0, s45
	global_load_lds_dwordx4 v2, s[26:27]
	s_mov_b32 m0, s48
	s_nop 0
	global_load_lds_dwordx4 v186, s[26:27]
	s_waitcnt vmcnt(8)
	s_waitcnt lgkmcnt(0)
	s_barrier
; template <class P, bool ALIGN_EPI>
; __device__ __forceinline__ void gemm_phase(ldsp lds, ldsp tab, const P& S) {
;     ...
;             for (int t = 2; t < nt; t += 2) PG8_TRIP(t, PG8_MMA);
;         } else {
;             for (int t = 0; t < nt; t += 2) PG8_TRIP(t, PG8_MMA);
	s_setprio 1
	s_waitcnt lgkmcnt(0)
	v_mfma_f32_16x16x32_bf16 v[144:147], v[100:103], v[164:167], v[144:147]
	v_mfma_f32_16x16x32_bf16 v[140:143], v[108:111], v[164:167], v[140:143]
	v_mfma_f32_16x16x32_bf16 v[136:139], v[100:103], v[172:175], v[136:139]
	v_mfma_f32_16x16x32_bf16 v[132:135], v[108:111], v[172:175], v[132:135]
	v_mfma_f32_16x16x32_bf16 v[128:131], v[100:103], v[180:183], v[128:131]
	v_mfma_f32_16x16x32_bf16 v[124:127], v[108:111], v[180:183], v[124:127]
	v_mfma_f32_16x16x32_bf16 v[120:123], v[100:103], v[194:197], v[120:123]
	v_mfma_f32_16x16x32_bf16 v[116:119], v[108:111], v[194:197], v[116:119]
	v_mfma_f32_16x16x32_bf16 v[144:147], v[104:107], v[168:171], v[144:147]
	v_mfma_f32_16x16x32_bf16 v[140:143], v[112:115], v[168:171], v[140:143]
	v_mfma_f32_16x16x32_bf16 v[136:139], v[104:107], v[176:179], v[136:139]
	v_mfma_f32_16x16x32_bf16 v[132:135], v[112:115], v[176:179], v[132:135]
	v_mfma_f32_16x16x32_bf16 v[128:131], v[104:107], v[190:193], v[128:131]
	v_mfma_f32_16x16x32_bf16 v[124:127], v[112:115], v[190:193], v[124:127]
	v_mfma_f32_16x16x32_bf16 v[120:123], v[104:107], v[198:201], v[120:123]
	v_mfma_f32_16x16x32_bf16 v[116:119], v[112:115], v[198:201], v[116:119]
	s_setprio 0
	s_setprio 1
	v_mfma_f32_16x16x32_bf16 v[68:71], v[148:151], v[164:167], v[68:71]
	v_mfma_f32_16x16x32_bf16 v[60:63], v[156:159], v[164:167], v[60:63]
	v_mfma_f32_16x16x32_bf16 v[56:59], v[148:151], v[172:175], v[56:59]
	v_mfma_f32_16x16x32_bf16 v[52:55], v[156:159], v[172:175], v[52:55]
	v_mfma_f32_16x16x32_bf16 v[48:51], v[148:151], v[180:183], v[48:51]
	v_mfma_f32_16x16x32_bf16 v[44:47], v[156:159], v[180:183], v[44:47]
	v_mfma_f32_16x16x32_bf16 v[40:43], v[148:151], v[194:197], v[40:43]
	v_mfma_f32_16x16x32_bf16 v[36:39], v[156:159], v[194:197], v[36:39]
	v_mfma_f32_16x16x32_bf16 v[68:71], v[152:155], v[168:171], v[68:71]
	v_mfma_f32_16x16x32_bf16 v[60:63], v[160:163], v[168:171], v[60:63]
	v_mfma_f32_16x16x32_bf16 v[56:59], v[152:155], v[176:179], v[56:59]
	v_mfma_f32_16x16x32_bf16 v[52:55], v[160:163], v[176:179], v[52:55]
	v_mfma_f32_16x16x32_bf16 v[48:51], v[152:155], v[190:193], v[48:51]
	v_mfma_f32_16x16x32_bf16 v[44:47], v[160:163], v[190:193], v[44:47]
	v_mfma_f32_16x16x32_bf16 v[40:43], v[152:155], v[198:201], v[40:43]
	v_mfma_f32_16x16x32_bf16 v[36:39], v[160:163], v[198:201], v[36:39]
	s_setprio 0
	s_barrier
	ds_read_b128 v[164:167], v249 offset:49152
	ds_read_b128 v[168:171], v249 offset:50176
	ds_read_b128 v[172:175], v249 offset:51200
	ds_read_b128 v[176:179], v249 offset:52224
	ds_read_b128 v[180:183], v249 offset:53248
	ds_read_b128 v[190:193], v249 offset:54272
	ds_read_b128 v[194:197], v249 offset:55296
	ds_read_b128 v[198:201], v249 offset:56320
	s_add_i32 s3, s3, s42
	v_lshl_add_u64 v[202:203], v[202:203], 0, s[24:25]
	s_mov_b32 m0, s3
	global_load_lds_dwordx4 v[202:203], off
	s_add_i32 m0, s3, 0x2000
	s_add_u32 s26, s30, 0xa0080
	v_lshl_add_u64 v[202:203], v[204:205], 0, s[24:25]
	s_addc_u32 s27, s31, 0
	s_add_i32 s3, s15, s42
	global_load_lds_dwordx4 v[202:203], off
	s_mov_b32 m0, s3
	v_lshl_add_u64 v[202:203], v[206:207], 0, s[24:25]
	global_load_lds_dwordx4 v184, s[26:27]
	s_add_i32 m0, s3, 0x2000
	s_nop 0
	global_load_lds_dwordx4 v188, s[26:27]
	s_mov_b32 m0, s50
	s_nop 0
	global_load_lds_dwordx4 v[202:203], off
	v_lshl_add_u64 v[202:203], v[208:209], 0, s[24:25]
	s_mov_b32 m0, s51
	s_nop 0
	global_load_lds_dwordx4 v[202:203], off
	s_waitcnt vmcnt(8)
	s_waitcnt lgkmcnt(0)
	s_barrier
	s_setprio 1
	s_waitcnt lgkmcnt(0)
	v_mfma_f32_16x16x32_bf16 v[96:99], v[100:103], v[164:167], v[96:99]
	v_mfma_f32_16x16x32_bf16 v[92:95], v[108:111], v[164:167], v[92:95]
	v_mfma_f32_16x16x32_bf16 v[88:91], v[100:103], v[172:175], v[88:91]
	v_mfma_f32_16x16x32_bf16 v[84:87], v[108:111], v[172:175], v[84:87]
	v_mfma_f32_16x16x32_bf16 v[80:83], v[100:103], v[180:183], v[80:83]
	v_mfma_f32_16x16x32_bf16 v[76:79], v[108:111], v[180:183], v[76:79]
	v_mfma_f32_16x16x32_bf16 v[72:75], v[100:103], v[194:197], v[72:75]
	v_mfma_f32_16x16x32_bf16 v[64:67], v[108:111], v[194:197], v[64:67]
	v_mfma_f32_16x16x32_bf16 v[96:99], v[104:107], v[168:171], v[96:99]
	v_mfma_f32_16x16x32_bf16 v[92:95], v[112:115], v[168:171], v[92:95]
	v_mfma_f32_16x16x32_bf16 v[88:91], v[104:107], v[176:179], v[88:91]
	v_mfma_f32_16x16x32_bf16 v[84:87], v[112:115], v[176:179], v[84:87]
	v_mfma_f32_16x16x32_bf16 v[80:83], v[104:107], v[190:193], v[80:83]
	v_mfma_f32_16x16x32_bf16 v[76:79], v[112:115], v[190:193], v[76:79]
	v_mfma_f32_16x16x32_bf16 v[72:75], v[104:107], v[198:201], v[72:75]
	v_mfma_f32_16x16x32_bf16 v[64:67], v[112:115], v[198:201], v[64:67]
	s_setprio 0
	s_setprio 1
	v_mfma_f32_16x16x32_bf16 v[32:35], v[148:151], v[164:167], v[32:35]
	v_mfma_f32_16x16x32_bf16 v[28:31], v[156:159], v[164:167], v[28:31]
	v_mfma_f32_16x16x32_bf16 v[24:27], v[148:151], v[172:175], v[24:27]
	v_mfma_f32_16x16x32_bf16 v[20:23], v[156:159], v[172:175], v[20:23]
	v_mfma_f32_16x16x32_bf16 v[16:19], v[148:151], v[180:183], v[16:19]
	v_mfma_f32_16x16x32_bf16 v[12:15], v[156:159], v[180:183], v[12:15]
	v_mfma_f32_16x16x32_bf16 v[8:11], v[148:151], v[194:197], v[8:11]
	v_mfma_f32_16x16x32_bf16 v[4:7], v[156:159], v[194:197], v[4:7]
	v_mfma_f32_16x16x32_bf16 v[32:35], v[152:155], v[168:171], v[32:35]
	v_mfma_f32_16x16x32_bf16 v[28:31], v[160:163], v[168:171], v[28:31]
	v_mfma_f32_16x16x32_bf16 v[24:27], v[152:155], v[176:179], v[24:27]
	v_mfma_f32_16x16x32_bf16 v[20:23], v[160:163], v[176:179], v[20:23]
	v_mfma_f32_16x16x32_bf16 v[16:19], v[152:155], v[190:193], v[16:19]
	v_mfma_f32_16x16x32_bf16 v[12:15], v[160:163], v[190:193], v[12:15]
	v_mfma_f32_16x16x32_bf16 v[8:11], v[152:155], v[198:201], v[8:11]
	v_mfma_f32_16x16x32_bf16 v[4:7], v[160:163], v[198:201], v[4:7]
	v_add_u32_e32 v112, 0x10000, v239
	v_add_u32_e32 v160, 0x14000, v239
	s_setprio 0
	s_barrier
	s_add_i32 s2, s2, 2
	s_add_u32 s22, s22, 0x100
	s_addc_u32 s23, s23, 0
	s_cmp_gt_u32 s2, 37
	s_cbranch_scc0 .LBB0_2007
	s_and_b64 vcc, exec, s[12:13]
	s_cbranch_vccz .LBB0_2010
	s_barrier
